# P1 K-loop LDS-DMA loads in saddr form (sgpr base + 32-bit vgpr offset + immediate): 16 fewer 64-bit VALU adds per iteration
# speedup vs baseline: 1.0149x; 1.0003x over previous
; #define PG8_STAGE(bufoff, gbase, voff) do { _Pragma("unroll") for (int _i = 0; _i < 2; ++_i) \
;         __builtin_amdgcn_global_load_lds((const unsigned*)((const char*)(gbase) + (voff)[_i]), (PG8_LAS unsigned*)(lds + (bufoff) + ldsw + _i * 8192), 16, 0, 0); } while (0)
; #define PG8_LDA(dst, b, h) do { _Pragma("unroll") for (int m = 0; m < 4; ++m) _Pragma("unroll") for (int k = 0; k < 2; ++k) dst[m][k] = *(const PG8_LAS bf16x8*)(lds + PG8_SA(b, h) + aoff + m * 2048 + k * 1024); } while (0)
; #define PG8_LDB(dst, b, h) do { _Pragma("unroll") for (int n = 0; n < 2; ++n) _Pragma("unroll") for (int k = 0; k < 2; ++k) dst[n][k] = *(const PG8_LAS bf16x8*)(lds + PG8_SB(b, h) + boff + n * 2048 + k * 1024); } while (0)
; #define PG8_MMA(ai, bj, At, Bt) do { __builtin_amdgcn_s_setprio(1); _Pragma("unroll") for (int m = 0; m < 4; ++m) _Pragma("unroll") for (int n = 0; n < 2; ++n) _Pragma("unroll") for (int k = 0; k < 2; ++k) \
;         acc[ai][bj][m][n] = __builtin_amdgcn_mfma_f32_16x16x32_bf16(Bt[n][k], At[m][k], acc[ai][bj][m][n], 0, 0, 0); __builtin_amdgcn_s_setprio(0); } while (0)
; #define PG8_WAIT_V(n) asm volatile("s_waitcnt vmcnt(" #n ")" ::: "memory")
; #define PG8_WAIT_L(n) asm volatile("s_waitcnt lgkmcnt(" #n ")" ::: "memory")
; #define PG8_BAR __builtin_amdgcn_s_barrier()
; #define PG8_SCHED __builtin_amdgcn_sched_barrier(0)
; template <class Epi, class Sched, bool ALIGN_EPI = false, bool SP2 = false>
; __device__ __forceinline__ void gemm_phase(PG8_LAS unsigned char* lds, const Gemm g, const Sched& S, const Epi& E) {
;     ...
;             const bool last = (t == nt - 2);
;             const char* a1 = cA + (size_t)(t + 1) * kstep;
;             const char* a2 = last ? nA : cA + (size_t)(t + 2) * kstep; const char* b2 = last ? nB : cB + (size_t)(t + 2) * kstep;
;             const char* a3 = a2 + kstep; const char* b3 = b2 + kstep;
;             if (last && has_next) S.a_ready(nxt);
;             if constexpr (SP2) {
;             PG8_LDB(B0, 0, 0); PG8_LDB(B1, 0, 1); PG8_SCHED; PG8_LDA(At, 0, 0); PG8_STAGEA(PG8_SA(1, 1), a1, 1, false);
;             PG8_WAIT_V(8); PG8_WAIT_L(0); PG8_BAR; PG8_MMA(0, 0, At, B0); PG8_MMA(0, 1, At, B1); PG8_BAR; PG8_SCHED;
;             PG8_LDA(At, 0, 1); PG8_STAGE(PG8_SB(0, 0), b2, voffB); PG8_STAGE(PG8_SB(0, 1), b2 + hstep, voffB); PG8_STAGEA(PG8_SA(0, 0), a2, 0, last);
.LBB0_110:
	v_add_u32_e32 v142, s79, v170
	v_add_u32_e32 v175, s80, v170
	ds_read_b128 v[130:133], v142
	ds_read_b128 v[134:137], v142 offset:1024
	ds_read_b128 v[138:141], v142 offset:2048
	ds_read_b128 v[142:145], v142 offset:3072
	ds_read_b128 v[162:165], v175
	ds_read_b128 v[166:169], v175 offset:1024
	ds_read_b128 v[176:179], v175 offset:2048
	ds_read_b128 v[180:183], v175 offset:3072
	s_add_u32 s54, s10, 0xfff80080
	s_addc_u32 s55, s11, -1
	s_cmp_eq_u32 s49, 28
	s_cselect_b32 s61, s9, s55
	s_cselect_b32 s60, s18, s54
	s_cselect_b32 s55, s19, s47
	s_cselect_b32 s54, s36, s37
	s_mov_b64 s[100:101], s[60:61]
	s_add_i32 m0, s57, 0xc000
	ds_read_b128 v[184:187], v174
	ds_read_b128 v[188:191], v174 offset:1024
	ds_read_b128 v[192:195], v174 offset:2048
	ds_read_b128 v[196:199], v174 offset:3072
	ds_read_b128 v[204:207], v174 offset:4096
	ds_read_b128 v[208:211], v174 offset:5120
	ds_read_b128 v[212:215], v174 offset:6144
	ds_read_b128 v[216:219], v174 offset:7168
	global_load_lds_dwordx4 v154, s[10:11]
	s_add_i32 m0, s57, 0xe000
	s_nop 0
	global_load_lds_dwordx4 v156, s[10:11]
	s_waitcnt vmcnt(8) lgkmcnt(0)
	s_barrier
	s_setprio 1
	v_mfma_f32_16x16x32_bf16 v[114:117], v[130:133], v[184:187], v[114:117]
	v_mfma_f32_16x16x32_bf16 v[118:121], v[138:141], v[184:187], v[118:121]
	v_mfma_f32_16x16x32_bf16 v[98:101], v[130:133], v[192:195], v[98:101]
	v_mfma_f32_16x16x32_bf16 v[102:105], v[138:141], v[192:195], v[102:105]
	v_mfma_f32_16x16x32_bf16 v[82:85], v[130:133], v[204:207], v[82:85]
	v_mfma_f32_16x16x32_bf16 v[86:89], v[138:141], v[204:207], v[86:89]
	v_mfma_f32_16x16x32_bf16 v[66:69], v[130:133], v[212:215], v[66:69]
	v_mfma_f32_16x16x32_bf16 v[70:73], v[138:141], v[212:215], v[70:73]
	v_mfma_f32_16x16x32_bf16 v[114:117], v[134:137], v[188:191], v[114:117]
	v_mfma_f32_16x16x32_bf16 v[118:121], v[142:145], v[188:191], v[118:121]
	v_mfma_f32_16x16x32_bf16 v[98:101], v[134:137], v[196:199], v[98:101]
	v_mfma_f32_16x16x32_bf16 v[102:105], v[142:145], v[196:199], v[102:105]
	v_mfma_f32_16x16x32_bf16 v[82:85], v[134:137], v[208:211], v[82:85]
	v_mfma_f32_16x16x32_bf16 v[86:89], v[142:145], v[208:211], v[86:89]
	v_mfma_f32_16x16x32_bf16 v[66:69], v[134:137], v[216:219], v[66:69]
	v_mfma_f32_16x16x32_bf16 v[70:73], v[142:145], v[216:219], v[70:73]
	v_mfma_f32_16x16x32_bf16 v[122:125], v[162:165], v[184:187], v[122:125]
	v_mfma_f32_16x16x32_bf16 v[126:129], v[176:179], v[184:187], v[126:129]
	v_mfma_f32_16x16x32_bf16 v[106:109], v[162:165], v[192:195], v[106:109]
	v_mfma_f32_16x16x32_bf16 v[110:113], v[176:179], v[192:195], v[110:113]
	v_mfma_f32_16x16x32_bf16 v[90:93], v[162:165], v[204:207], v[90:93]
	v_mfma_f32_16x16x32_bf16 v[94:97], v[176:179], v[204:207], v[94:97]
	v_mfma_f32_16x16x32_bf16 v[74:77], v[162:165], v[212:215], v[74:77]
	v_mfma_f32_16x16x32_bf16 v[78:81], v[176:179], v[212:215], v[78:81]
	v_mfma_f32_16x16x32_bf16 v[122:125], v[166:169], v[188:191], v[122:125]
	v_mfma_f32_16x16x32_bf16 v[126:129], v[180:183], v[188:191], v[126:129]
	v_mfma_f32_16x16x32_bf16 v[106:109], v[166:169], v[196:199], v[106:109]
	v_mfma_f32_16x16x32_bf16 v[110:113], v[180:183], v[196:199], v[110:113]
	v_mfma_f32_16x16x32_bf16 v[90:93], v[166:169], v[208:211], v[90:93]
	v_mfma_f32_16x16x32_bf16 v[94:97], v[180:183], v[208:211], v[94:97]
	v_mfma_f32_16x16x32_bf16 v[74:77], v[166:169], v[216:219], v[74:77]
	v_mfma_f32_16x16x32_bf16 v[78:81], v[180:183], v[216:219], v[78:81]
	s_setprio 0
	s_barrier
	s_add_i32 s59, s79, s66
	s_mov_b32 m0, s59
	ds_read_b128 v[184:187], v174 offset:16384
	ds_read_b128 v[188:191], v174 offset:17408
	ds_read_b128 v[192:195], v174 offset:18432
	ds_read_b128 v[196:199], v174 offset:19456
	ds_read_b128 v[204:207], v174 offset:20480
	ds_read_b128 v[208:211], v174 offset:21504
	ds_read_b128 v[212:215], v174 offset:22528
	ds_read_b128 v[216:219], v174 offset:23552
	global_load_lds_dwordx4 v148, s[54:55]
	s_add_i32 m0, s59, 0x2000
	s_add_u32 s62, s54, 0x80000
	s_addc_u32 s63, s55, 0
	s_add_i32 s59, s80, s66
	global_load_lds_dwordx4 v152, s[54:55]
	s_mov_b32 m0, s59
	s_nop 0
	global_load_lds_dwordx4 v148, s[62:63]
	s_add_i32 m0, s59, 0x2000
	s_nop 0
	global_load_lds_dwordx4 v152, s[62:63]
	s_mov_b32 m0, s57
	s_nop 0
	global_load_lds_dwordx4 v146, s[60:61]
	s_mov_b32 m0, s67
	s_nop 0
	global_load_lds_dwordx4 v150, s[60:61]
	s_waitcnt vmcnt(8) lgkmcnt(0)
	s_barrier
	s_setprio 1
	v_mfma_f32_16x16x32_bf16 v[58:61], v[130:133], v[184:187], v[58:61]
	v_mfma_f32_16x16x32_bf16 v[62:65], v[138:141], v[184:187], v[62:65]
	v_mfma_f32_16x16x32_bf16 v[42:45], v[130:133], v[192:195], v[42:45]
	v_mfma_f32_16x16x32_bf16 v[46:49], v[138:141], v[192:195], v[46:49]
	v_mfma_f32_16x16x32_bf16 v[18:21], v[130:133], v[204:207], v[18:21]
	v_mfma_f32_16x16x32_bf16 v[22:25], v[138:141], v[204:207], v[22:25]
	v_mfma_f32_16x16x32_bf16 v[6:9], v[130:133], v[212:215], v[6:9]
	v_mfma_f32_16x16x32_bf16 v[14:17], v[138:141], v[212:215], v[14:17]
	v_mfma_f32_16x16x32_bf16 v[58:61], v[134:137], v[188:191], v[58:61]
	v_mfma_f32_16x16x32_bf16 v[62:65], v[142:145], v[188:191], v[62:65]
	v_mfma_f32_16x16x32_bf16 v[42:45], v[134:137], v[196:199], v[42:45]
	v_mfma_f32_16x16x32_bf16 v[46:49], v[142:145], v[196:199], v[46:49]
	v_mfma_f32_16x16x32_bf16 v[18:21], v[134:137], v[208:211], v[18:21]
	v_mfma_f32_16x16x32_bf16 v[22:25], v[142:145], v[208:211], v[22:25]
	v_mfma_f32_16x16x32_bf16 v[6:9], v[134:137], v[216:219], v[6:9]
	v_mfma_f32_16x16x32_bf16 v[14:17], v[142:145], v[216:219], v[14:17]
	v_mfma_f32_16x16x32_bf16 v[50:53], v[162:165], v[184:187], v[50:53]
	v_mfma_f32_16x16x32_bf16 v[54:57], v[176:179], v[184:187], v[54:57]
	v_mfma_f32_16x16x32_bf16 v[34:37], v[162:165], v[192:195], v[34:37]
	v_mfma_f32_16x16x32_bf16 v[38:41], v[176:179], v[192:195], v[38:41]
	v_mfma_f32_16x16x32_bf16 v[26:29], v[162:165], v[204:207], v[26:29]
	v_mfma_f32_16x16x32_bf16 v[30:33], v[176:179], v[204:207], v[30:33]
	v_mfma_f32_16x16x32_bf16 v[10:13], v[162:165], v[212:215], v[10:13]
	v_mfma_f32_16x16x32_bf16 v[2:5], v[176:179], v[212:215], v[2:5]
	v_mfma_f32_16x16x32_bf16 v[50:53], v[166:169], v[188:191], v[50:53]
	v_mfma_f32_16x16x32_bf16 v[54:57], v[180:183], v[188:191], v[54:57]
	v_mfma_f32_16x16x32_bf16 v[34:37], v[166:169], v[196:199], v[34:37]
	v_mfma_f32_16x16x32_bf16 v[38:41], v[180:183], v[196:199], v[38:41]
	v_mfma_f32_16x16x32_bf16 v[26:29], v[166:169], v[208:211], v[26:29]
	v_mfma_f32_16x16x32_bf16 v[30:33], v[180:183], v[208:211], v[30:33]
	v_mfma_f32_16x16x32_bf16 v[10:13], v[166:169], v[216:219], v[10:13]
	v_mfma_f32_16x16x32_bf16 v[2:5], v[180:183], v[216:219], v[2:5]
	s_setprio 0
	s_barrier
; #define PG8_STAGE(bufoff, gbase, voff) do { _Pragma("unroll") for (int _i = 0; _i < 2; ++_i) \
;         __builtin_amdgcn_global_load_lds((const unsigned*)((const char*)(gbase) + (voff)[_i]), (PG8_LAS unsigned*)(lds + (bufoff) + ldsw + _i * 8192), 16, 0, 0); } while (0)
; #define PG8_LDA(dst, b, h) do { _Pragma("unroll") for (int m = 0; m < 4; ++m) _Pragma("unroll") for (int k = 0; k < 2; ++k) dst[m][k] = *(const PG8_LAS bf16x8*)(lds + PG8_SA(b, h) + aoff + m * 2048 + k * 1024); } while (0)
; #define PG8_LDB(dst, b, h) do { _Pragma("unroll") for (int n = 0; n < 2; ++n) _Pragma("unroll") for (int k = 0; k < 2; ++k) dst[n][k] = *(const PG8_LAS bf16x8*)(lds + PG8_SB(b, h) + boff + n * 2048 + k * 1024); } while (0)
; #define PG8_MMA(ai, bj, At, Bt) do { __builtin_amdgcn_s_setprio(1); _Pragma("unroll") for (int m = 0; m < 4; ++m) _Pragma("unroll") for (int n = 0; n < 2; ++n) _Pragma("unroll") for (int k = 0; k < 2; ++k) \
;         acc[ai][bj][m][n] = __builtin_amdgcn_mfma_f32_16x16x32_bf16(Bt[n][k], At[m][k], acc[ai][bj][m][n], 0, 0, 0); __builtin_amdgcn_s_setprio(0); } while (0)
; #define PG8_WAIT_V(n) asm volatile("s_waitcnt vmcnt(" #n ")" ::: "memory")
; #define PG8_WAIT_L(n) asm volatile("s_waitcnt lgkmcnt(" #n ")" ::: "memory")
; #define PG8_BAR __builtin_amdgcn_s_barrier()
; #define PG8_SCHED __builtin_amdgcn_sched_barrier(0)
; template <class Epi, class Sched, bool ALIGN_EPI = false, bool SP2 = false>
; __device__ __forceinline__ void gemm_phase(PG8_LAS unsigned char* lds, const Gemm g, const Sched& S, const Epi& E) {
;     ...
;             PG8_WAIT_V(8); PG8_WAIT_L(0); PG8_BAR; PG8_MMA(1, 0, At, B0); PG8_MMA(1, 1, At, B1); PG8_BAR; PG8_SCHED;
;             PG8_LDB(B0, 1, 0); PG8_LDB(B1, 1, 1); PG8_SCHED; PG8_LDA(At, 1, 0); PG8_STAGEA(PG8_SA(0, 1), a2, 1, last);
;             PG8_WAIT_V(8); PG8_WAIT_L(0); PG8_BAR; PG8_MMA(0, 0, At, B0); PG8_MMA(0, 1, At, B1); PG8_BAR; PG8_SCHED;
;             PG8_LDA(At, 1, 1); PG8_STAGE(PG8_SB(1, 0), b3, voffB); PG8_STAGE(PG8_SB(1, 1), b3 + hstep, voffB); PG8_STAGEA(PG8_SA(1, 0), a3, 0, last);
;             PG8_WAIT_V(8); PG8_WAIT_L(0); PG8_BAR; PG8_MMA(1, 0, At, B0); PG8_MMA(1, 1, At, B1); PG8_BAR; PG8_SCHED;
	s_add_i32 s59, 0, 0x18000
	s_add_i32 s62, 0, 0x1c000
	v_add_u32_e32 v142, s59, v170
	v_add_u32_e32 v175, s62, v170
	ds_read_b128 v[130:133], v142
	ds_read_b128 v[134:137], v142 offset:1024
	ds_read_b128 v[138:141], v142 offset:2048
	ds_read_b128 v[142:145], v142 offset:3072
	ds_read_b128 v[162:165], v175
	ds_read_b128 v[166:169], v175 offset:1024
	ds_read_b128 v[176:179], v175 offset:2048
	ds_read_b128 v[180:183], v175 offset:3072
	s_add_u32 s60, s60, 0x80000
	s_addc_u32 s61, s61, 0
	s_mov_b32 m0, s68
	ds_read_b128 v[184:187], v174 offset:32768
	ds_read_b128 v[188:191], v174 offset:33792
	ds_read_b128 v[192:195], v174 offset:34816
	ds_read_b128 v[196:199], v174 offset:35840
	ds_read_b128 v[204:207], v174 offset:36864
	ds_read_b128 v[208:211], v174 offset:37888
	ds_read_b128 v[212:215], v174 offset:38912
	ds_read_b128 v[216:219], v174 offset:39936
	global_load_lds_dwordx4 v146, s[60:61]
	s_mov_b32 m0, s69
	s_nop 0
	global_load_lds_dwordx4 v150, s[60:61]
	s_waitcnt vmcnt(8) lgkmcnt(0)
	s_barrier
	s_setprio 1
	v_mfma_f32_16x16x32_bf16 v[114:117], v[130:133], v[184:187], v[114:117]
	v_mfma_f32_16x16x32_bf16 v[118:121], v[138:141], v[184:187], v[118:121]
	v_mfma_f32_16x16x32_bf16 v[98:101], v[130:133], v[192:195], v[98:101]
	v_mfma_f32_16x16x32_bf16 v[102:105], v[138:141], v[192:195], v[102:105]
	v_mfma_f32_16x16x32_bf16 v[82:85], v[130:133], v[204:207], v[82:85]
	v_mfma_f32_16x16x32_bf16 v[86:89], v[138:141], v[204:207], v[86:89]
	v_mfma_f32_16x16x32_bf16 v[66:69], v[130:133], v[212:215], v[66:69]
	v_mfma_f32_16x16x32_bf16 v[70:73], v[138:141], v[212:215], v[70:73]
	v_mfma_f32_16x16x32_bf16 v[114:117], v[134:137], v[188:191], v[114:117]
	v_mfma_f32_16x16x32_bf16 v[118:121], v[142:145], v[188:191], v[118:121]
	v_mfma_f32_16x16x32_bf16 v[98:101], v[134:137], v[196:199], v[98:101]
	v_mfma_f32_16x16x32_bf16 v[102:105], v[142:145], v[196:199], v[102:105]
	v_mfma_f32_16x16x32_bf16 v[82:85], v[134:137], v[208:211], v[82:85]
	v_mfma_f32_16x16x32_bf16 v[86:89], v[142:145], v[208:211], v[86:89]
	v_mfma_f32_16x16x32_bf16 v[66:69], v[134:137], v[216:219], v[66:69]
	v_mfma_f32_16x16x32_bf16 v[70:73], v[142:145], v[216:219], v[70:73]
	v_mfma_f32_16x16x32_bf16 v[122:125], v[162:165], v[184:187], v[122:125]
	v_mfma_f32_16x16x32_bf16 v[126:129], v[176:179], v[184:187], v[126:129]
	v_mfma_f32_16x16x32_bf16 v[106:109], v[162:165], v[192:195], v[106:109]
	v_mfma_f32_16x16x32_bf16 v[110:113], v[176:179], v[192:195], v[110:113]
	v_mfma_f32_16x16x32_bf16 v[90:93], v[162:165], v[204:207], v[90:93]
	v_mfma_f32_16x16x32_bf16 v[94:97], v[176:179], v[204:207], v[94:97]
	v_mfma_f32_16x16x32_bf16 v[74:77], v[162:165], v[212:215], v[74:77]
	v_mfma_f32_16x16x32_bf16 v[78:81], v[176:179], v[212:215], v[78:81]
	v_mfma_f32_16x16x32_bf16 v[122:125], v[166:169], v[188:191], v[122:125]
	v_mfma_f32_16x16x32_bf16 v[126:129], v[180:183], v[188:191], v[126:129]
	v_mfma_f32_16x16x32_bf16 v[106:109], v[166:169], v[196:199], v[106:109]
	v_mfma_f32_16x16x32_bf16 v[110:113], v[180:183], v[196:199], v[110:113]
	v_mfma_f32_16x16x32_bf16 v[90:93], v[166:169], v[208:211], v[90:93]
	v_mfma_f32_16x16x32_bf16 v[94:97], v[180:183], v[208:211], v[94:97]
	v_mfma_f32_16x16x32_bf16 v[74:77], v[166:169], v[216:219], v[74:77]
	v_mfma_f32_16x16x32_bf16 v[78:81], v[180:183], v[216:219], v[78:81]
	s_setprio 0
	s_barrier
	s_add_i32 s59, s59, s66
	s_add_i32 m0, s59, 0xffffff80
	ds_read_b128 v[184:187], v174 offset:49152
	ds_read_b128 v[188:191], v174 offset:50176
	ds_read_b128 v[192:195], v174 offset:51200
	ds_read_b128 v[196:199], v174 offset:52224
	ds_read_b128 v[204:207], v174 offset:53248
	ds_read_b128 v[208:211], v174 offset:54272
	ds_read_b128 v[212:215], v174 offset:55296
	ds_read_b128 v[216:219], v174 offset:56320
	global_load_lds_dwordx4 v148, s[54:55] offset:128
	s_add_i32 m0, s59, 0x1f80
	s_add_i32 s59, s62, s66
	global_load_lds_dwordx4 v152, s[54:55] offset:128
	s_add_u32 s54, s54, 0x80080
	s_addc_u32 s55, s55, 0
	s_mov_b32 m0, s59
	s_nop 0
	global_load_lds_dwordx4 v148, s[54:55]
	s_add_i32 m0, s59, 0x2000
	s_nop 0
	global_load_lds_dwordx4 v152, s[54:55]
	s_add_i32 m0, s74, 0xffffff80
	s_nop 0
	global_load_lds_dwordx4 v146, s[100:101] offset:128
	s_add_i32 m0, s75, 0xffffff80
	s_nop 0
	global_load_lds_dwordx4 v150, s[100:101] offset:128
	s_waitcnt vmcnt(8) lgkmcnt(0)
	s_barrier
	s_setprio 1
	v_mfma_f32_16x16x32_bf16 v[58:61], v[130:133], v[184:187], v[58:61]
	v_mfma_f32_16x16x32_bf16 v[62:65], v[138:141], v[184:187], v[62:65]
	v_mfma_f32_16x16x32_bf16 v[42:45], v[130:133], v[192:195], v[42:45]
	v_mfma_f32_16x16x32_bf16 v[46:49], v[138:141], v[192:195], v[46:49]
	v_mfma_f32_16x16x32_bf16 v[18:21], v[130:133], v[204:207], v[18:21]
	v_mfma_f32_16x16x32_bf16 v[22:25], v[138:141], v[204:207], v[22:25]
	v_mfma_f32_16x16x32_bf16 v[6:9], v[130:133], v[212:215], v[6:9]
	v_mfma_f32_16x16x32_bf16 v[14:17], v[138:141], v[212:215], v[14:17]
	v_mfma_f32_16x16x32_bf16 v[58:61], v[134:137], v[188:191], v[58:61]
	v_mfma_f32_16x16x32_bf16 v[62:65], v[142:145], v[188:191], v[62:65]
	v_mfma_f32_16x16x32_bf16 v[42:45], v[134:137], v[196:199], v[42:45]
	v_mfma_f32_16x16x32_bf16 v[46:49], v[142:145], v[196:199], v[46:49]
	v_mfma_f32_16x16x32_bf16 v[18:21], v[134:137], v[208:211], v[18:21]
	v_mfma_f32_16x16x32_bf16 v[22:25], v[142:145], v[208:211], v[22:25]
	v_mfma_f32_16x16x32_bf16 v[6:9], v[134:137], v[216:219], v[6:9]
	v_mfma_f32_16x16x32_bf16 v[14:17], v[142:145], v[216:219], v[14:17]
	v_mfma_f32_16x16x32_bf16 v[50:53], v[162:165], v[184:187], v[50:53]
	v_mfma_f32_16x16x32_bf16 v[54:57], v[176:179], v[184:187], v[54:57]
	v_mfma_f32_16x16x32_bf16 v[34:37], v[162:165], v[192:195], v[34:37]
	v_mfma_f32_16x16x32_bf16 v[38:41], v[176:179], v[192:195], v[38:41]
	v_mfma_f32_16x16x32_bf16 v[26:29], v[162:165], v[204:207], v[26:29]
	v_mfma_f32_16x16x32_bf16 v[30:33], v[176:179], v[204:207], v[30:33]
	v_mfma_f32_16x16x32_bf16 v[10:13], v[162:165], v[212:215], v[10:13]
	v_mfma_f32_16x16x32_bf16 v[2:5], v[176:179], v[212:215], v[2:5]
	v_mfma_f32_16x16x32_bf16 v[50:53], v[166:169], v[188:191], v[50:53]
	v_mfma_f32_16x16x32_bf16 v[54:57], v[180:183], v[188:191], v[54:57]
	v_mfma_f32_16x16x32_bf16 v[34:37], v[166:169], v[196:199], v[34:37]
	v_mfma_f32_16x16x32_bf16 v[38:41], v[180:183], v[196:199], v[38:41]
	v_mfma_f32_16x16x32_bf16 v[26:29], v[166:169], v[208:211], v[26:29]
	v_mfma_f32_16x16x32_bf16 v[30:33], v[180:183], v[208:211], v[30:33]
	v_mfma_f32_16x16x32_bf16 v[10:13], v[166:169], v[216:219], v[10:13]
	v_mfma_f32_16x16x32_bf16 v[2:5], v[180:183], v[216:219], v[2:5]
	s_setprio 0
	s_barrier
	s_add_i32 s49, s49, 2
	s_add_u32 s10, s10, 0x100
	s_addc_u32 s11, s11, 0
	s_add_u32 s37, s37, 0x100
	s_addc_u32 s47, s47, 0
	s_cmp_gt_u32 s49, 29
	s_cbranch_scc0 .LBB0_110
	s_and_b64 vcc, exec, s[38:39]
	s_cbranch_vccz .LBB0_113
	s_barrier
